# same design with a 10-deep load ring per scanner wave instead of 20
# baseline (speedup 1.0000x reference)
_Z11attn_kernelPKfS0_PKDv8_DF16_S0_Pfi:
	s_load_dwordx2 s[28:29], s[0:1], 0x0
	v_cmp_gt_u32_e32 vcc, 8, v0
	s_and_saveexec_b64 s[4:5], vcc
	v_lshlrev_b32_e32 v1, 2, v0
	v_mov_b32_e32 v2, 0
	ds_write_b32 v1, v2 offset:36864
	s_or_b64 exec, exec, s[4:5]
	s_load_dword s33, s[0:1], 0x28
	v_bfe_u32 v1, v0, 6, 2
	v_lshl_or_b32 v82, s2, 2, v1
	v_readfirstlane_b32 s34, v0
	s_cmp_gt_u32 s34, 0xff
	s_cbranch_scc1 .Lsc_early_skip
	v_and_b32_e32 v3, 63, v0
	v_lshlrev_b32_e32 v2, 4, v3
	s_lshr_b32 s35, s34, 6
	s_lshl_b32 s37, s2, 2
	s_add_u32 s37, s37, s35
	s_and_b32 s47, s37, 1
	s_lshl_b32 s47, s47, 2
	s_mul_i32 s38, s37, 0x9c40
	s_lshl_b32 s40, s47, 4
	s_sub_u32 s38, s38, s40
	v_max_u32_e32 v12, s47, v3
	v_lshlrev_b32_e32 v12, 4, v12
	s_waitcnt lgkmcnt(0)
	s_and_b32 s29, s29, 0xffff
	s_mov_b32 s30, 0x17d78400
	s_mov_b32 s31, 0x20000
	buffer_load_dwordx4 v[100:103], v12, s[28:31], s38 offen nt
	s_add_u32 s40, s38, 0x400
	buffer_load_dwordx4 v[104:107], v2, s[28:31], s40 offen nt
	s_add_u32 s40, s38, 0x800
	buffer_load_dwordx4 v[108:111], v2, s[28:31], s40 offen nt
	s_add_u32 s40, s38, 0xc00
	buffer_load_dwordx4 v[112:115], v2, s[28:31], s40 offen nt
	s_add_u32 s40, s38, 0x1000
	buffer_load_dwordx4 v[116:119], v2, s[28:31], s40 offen nt
	s_add_u32 s40, s38, 0x1400
	buffer_load_dwordx4 v[120:123], v2, s[28:31], s40 offen nt
	s_add_u32 s40, s38, 0x1800
	buffer_load_dwordx4 v[124:127], v2, s[28:31], s40 offen nt
	s_add_u32 s40, s38, 0x1c00
	buffer_load_dwordx4 v[128:131], v2, s[28:31], s40 offen nt
	s_add_u32 s40, s38, 0x2000
	buffer_load_dwordx4 v[132:135], v2, s[28:31], s40 offen nt
	s_add_u32 s40, s38, 0x2400
	buffer_load_dwordx4 v[136:139], v2, s[28:31], s40 offen nt
.Lsc_early_skip:
	s_waitcnt lgkmcnt(0)
	s_barrier
	v_cmp_gt_i32_e32 vcc, s33, v82
	s_and_saveexec_b64 s[4:5], vcc
	s_cbranch_execz .LBB1_384
	s_abs_i32 s3, s33
	v_cvt_f32_u32_e32 v2, s3
	s_movk_i32 s4, 0xff
	v_sub_u32_e32 v3, 0x270f, v82
	v_cmp_lt_u32_e32 vcc, s4, v0
	v_rcp_iflag_f32_e32 v2, v2
	v_sub_u32_e32 v5, 0, v3
	s_sub_i32 s4, 0, s3
	v_xor_b32_e32 v4, s33, v3
	v_mul_f32_e32 v2, 0x4f7ffffe, v2
	v_cvt_u32_f32_e32 v2, v2
	v_max_i32_e32 v3, v3, v5
	v_ashrrev_i32_e32 v4, 31, v4
	v_mul_lo_u32 v5, s4, v2
	v_mul_hi_u32 v5, v2, v5
	v_add_u32_e32 v2, v2, v5
	v_mul_hi_u32 v2, v3, v2
	v_mul_lo_u32 v5, v2, s3
	v_sub_u32_e32 v3, v3, v5
	v_add_u32_e32 v5, 1, v2
	v_cmp_le_u32_e64 s[4:5], s3, v3
	v_and_b32_e32 v83, 63, v0
	s_nop 0
	v_cndmask_b32_e64 v2, v2, v5, s[4:5]
	v_subrev_u32_e32 v5, s3, v3
	v_cndmask_b32_e64 v3, v3, v5, s[4:5]
	v_add_u32_e32 v5, 1, v2
	v_cmp_le_u32_e64 s[4:5], s3, v3
	s_nop 1
	v_cndmask_b32_e64 v2, v2, v5, s[4:5]
	v_xor_b32_e32 v2, v2, v4
	v_sub_u32_e32 v84, v2, v4
	s_and_saveexec_b64 s[4:5], vcc
	s_xor_b64 s[30:31], exec, s[4:5]
	s_cbranch_execz .LBB1_217
	v_cmp_lt_i32_e32 vcc, -1, v84
	s_and_saveexec_b64 s[34:35], vcc
	s_cbranch_execz .LBB1_216
	s_load_dwordx8 s[20:27], s[0:1], 0x8
	v_and_b32_e32 v69, 15, v0
	v_mov_b32_e32 v0, 0x8000
	v_lshrrev_b32_e32 v67, 4, v83
	v_lshl_or_b32 v88, v1, 10, v0
	s_mul_i32 s3, s2, 0x2710
	v_mul_u32_u24_e32 v0, 0x9c4, v1
	v_lshl_or_b32 v89, v69, 2, v67
	v_add3_u32 v90, s3, v0, v83
	v_lshlrev_b32_e32 v0, 2, v1
	v_mov_b32_e32 v2, 0x9000
	v_lshl_or_b32 v91, s2, 4, v0
	v_lshlrev_b32_e32 v0, 3, v89
	v_mov_b32_e32 v32, 0
	v_lshl_or_b32 v65, v1, 3, v2
	v_or_b32_e32 v2, 0x1e00, v0
	v_mov_b32_e32 v3, v32
	s_waitcnt lgkmcnt(0)
	v_lshl_add_u64 v[34:35], s[20:21], 0, v[2:3]
	v_or_b32_e32 v2, 0x1c00, v0
	v_lshl_add_u64 v[36:37], s[20:21], 0, v[2:3]
	v_or_b32_e32 v2, 0x1a00, v0
	v_lshl_add_u64 v[38:39], s[20:21], 0, v[2:3]
	v_or_b32_e32 v2, 0x1800, v0
	v_lshl_add_u64 v[40:41], s[20:21], 0, v[2:3]
	v_or_b32_e32 v2, 0x1600, v0
	v_lshl_add_u64 v[42:43], s[20:21], 0, v[2:3]
	v_or_b32_e32 v2, 0x1400, v0
	v_lshlrev_b32_e32 v63, 12, v1
	v_lshl_add_u64 v[44:45], s[20:21], 0, v[2:3]
	v_or_b32_e32 v2, 0x1200, v0
	v_mov_b32_e32 v1, v32
	v_lshl_or_b32 v71, v83, 3, v63
	v_lshl_or_b32 v73, v67, 3, v63
	v_lshl_add_u64 v[46:47], s[20:21], 0, v[2:3]
	v_or_b32_e32 v2, 0x1000, v0
	v_lshl_add_u64 v[50:51], s[20:21], 0, v[0:1]
	v_mbcnt_lo_u32_b32 v0, -1, 0
	v_or_b32_e32 v75, 4, v67
	v_or_b32_e32 v77, 8, v67
	v_or_b32_e32 v78, 12, v67
	v_or_b32_e32 v79, 16, v67
	v_or_b32_e32 v80, 20, v67
	v_or_b32_e32 v81, 24, v67
	v_or_b32_e32 v85, 28, v67
	v_or_b32_e32 v86, 64, v83
	v_or_b32_e32 v87, 0x4000, v63
	v_cmp_lt_u32_e64 s[0:1], 15, v83
	s_mul_i32 s39, s33, 0x9c4
	s_lshl_b32 s48, s33, 2
	v_or_b32_e32 v92, 0x200, v71
	v_or_b32_e32 v93, 0x204, v71
	v_or_b32_e32 v94, 0x100, v73
	v_lshl_add_u64 v[48:49], s[20:21], 0, v[2:3]
	s_mov_b32 s51, 0
	s_mov_b64 s[36:37], 0
	s_movk_i32 s49, 0x81
	s_mov_b32 s50, 0xff800000
	s_mov_b32 s38, 0x38d1b717
	v_mov_b32_e32 v95, 0xff800000
	v_mbcnt_hi_u32_b32 v96, -1, v0
	v_mov_b32_e32 v136, 0
	v_mov_b32_e32 v137, 0
	v_mov_b32_e32 v138, 0
	v_mov_b32_e32 v139, 0
	v_mov_b32_e32 v140, 0
	v_mov_b32_e32 v141, 0
	v_mov_b32_e32 v142, 0
	v_mov_b32_e32 v143, 0
	v_mov_b32_e32 v144, 0
	v_mov_b32_e32 v145, 0
	v_mov_b32_e32 v146, 0
	v_mov_b32_e32 v147, 0
	v_mov_b32_e32 v148, 0
	v_mov_b32_e32 v149, 0
	v_mov_b32_e32 v150, 0
	v_mov_b32_e32 v151, 0
	v_mov_b32_e32 v152, 0
	v_mov_b32_e32 v153, 0
	v_mov_b32_e32 v154, 0
	v_mov_b32_e32 v155, 0
	v_mov_b32_e32 v156, 0
	v_mov_b32_e32 v157, 0
	v_mov_b32_e32 v158, 0
	v_mov_b32_e32 v159, 0
	v_mov_b32_e32 v160, 0
	v_mov_b32_e32 v161, 0
	v_mov_b32_e32 v162, 0
	v_mov_b32_e32 v163, 0
	v_mov_b32_e32 v164, 0
	v_mov_b32_e32 v165, 0
	v_mov_b32_e32 v166, 0
	v_mov_b32_e32 v167, 0
	v_mov_b32_e32 v168, 0
	v_mov_b32_e32 v169, 0
	v_mov_b32_e32 v170, 0
	v_mov_b32_e32 v171, 0
	v_mov_b32_e32 v172, 0
	v_mov_b32_e32 v173, 0
	v_mov_b32_e32 v174, 0
	v_mov_b32_e32 v175, 0
	v_mov_b32_e32 v176, 0
	v_mov_b32_e32 v177, 0
	v_mov_b32_e32 v178, 0
	v_mov_b32_e32 v179, 0
	v_mov_b32_e32 v180, 0
	v_mov_b32_e32 v181, 0
	v_mov_b32_e32 v182, 0
	v_mov_b32_e32 v183, 0
	v_mov_b32_e32 v184, 0
	v_mov_b32_e32 v185, 0
	v_mov_b32_e32 v186, 0
	v_mov_b32_e32 v187, 0
	v_mov_b32_e32 v188, 0
	v_mov_b32_e32 v189, 0
	v_mov_b32_e32 v190, 0
	v_mov_b32_e32 v191, 0
	v_mov_b32_e32 v192, 0
	v_mov_b32_e32 v193, 0
	v_mov_b32_e32 v194, 0
	v_mov_b32_e32 v195, 0
	v_mov_b32_e32 v196, 0
	v_mov_b32_e32 v197, 0
	v_mov_b32_e32 v198, 0
	v_mov_b32_e32 v199, 0
	s_branch .LBB1_9

.Lsc_go:
	s_mov_b32 s42, 0
	s_waitcnt vmcnt(9)
	v_or3_b32 v12, v100, v101, v102
	v_bitop3_b32 v12, v12, s9, v103 bitop3:0xc8
	v_cmp_ne_u32_e32 vcc, 0, v12
	s_and_b64 vcc, vcc, s[48:49]
	s_cbranch_vccz .Lsc_s0
	s_nop 0
	v_mbcnt_lo_u32_b32 v13, vcc_lo, 0
	v_mbcnt_hi_u32_b32 v13, vcc_hi, v13
	v_add_u32_e32 v13, s42, v13
	v_cmp_gt_i32_e64 s[0:1], s7, v13
	s_and_b64 s[4:5], vcc, s[0:1]
	s_and_saveexec_b64 s[0:1], s[4:5]
	v_lshl_add_u32 v14, v13, 4, v9
	v_lshl_add_u32 v15, v13, 2, v10
	v_mov_b32_e32 v13, v8
	ds_write_b128 v14, v[100:103]
	ds_write_b32 v15, v13
	s_mov_b64 exec, -1
	s_bcnt1_i32_b64 s40, vcc
	s_add_i32 s42, s42, s40
.Lsc_s0:
	s_add_u32 s40, s38, 0x2800
	buffer_load_dwordx4 v[100:103], v2, s[28:31], s40 offen nt
	s_waitcnt vmcnt(9)
	v_or3_b32 v12, v104, v105, v106
	v_bitop3_b32 v12, v12, s9, v107 bitop3:0xc8
	v_cmp_ne_u32_e32 vcc, 0, v12
	s_cbranch_vccz .Lsc_s1
	s_nop 0
	v_mbcnt_lo_u32_b32 v13, vcc_lo, 0
	v_mbcnt_hi_u32_b32 v13, vcc_hi, v13
	v_add_u32_e32 v13, s42, v13
	v_cmp_gt_i32_e64 s[0:1], s7, v13
	s_and_b64 s[4:5], vcc, s[0:1]
	s_and_saveexec_b64 s[0:1], s[4:5]
	v_lshl_add_u32 v14, v13, 4, v9
	v_lshl_add_u32 v15, v13, 2, v10
	v_add_u32_e32 v13, 0x100, v8
	ds_write_b128 v14, v[104:107]
	ds_write_b32 v15, v13
	s_mov_b64 exec, -1
	s_bcnt1_i32_b64 s40, vcc
	s_add_i32 s42, s42, s40
.Lsc_s1:
	s_add_u32 s40, s38, 0x2c00
	buffer_load_dwordx4 v[104:107], v2, s[28:31], s40 offen nt
	s_waitcnt vmcnt(9)
	v_or3_b32 v12, v108, v109, v110
	v_bitop3_b32 v12, v12, s9, v111 bitop3:0xc8
	v_cmp_ne_u32_e32 vcc, 0, v12
	s_cbranch_vccz .Lsc_s2
	s_nop 0
	v_mbcnt_lo_u32_b32 v13, vcc_lo, 0
	v_mbcnt_hi_u32_b32 v13, vcc_hi, v13
	v_add_u32_e32 v13, s42, v13
	v_cmp_gt_i32_e64 s[0:1], s7, v13
	s_and_b64 s[4:5], vcc, s[0:1]
	s_and_saveexec_b64 s[0:1], s[4:5]
	v_lshl_add_u32 v14, v13, 4, v9
	v_lshl_add_u32 v15, v13, 2, v10
	v_add_u32_e32 v13, 0x200, v8
	ds_write_b128 v14, v[108:111]
	ds_write_b32 v15, v13
	s_mov_b64 exec, -1
	s_bcnt1_i32_b64 s40, vcc
	s_add_i32 s42, s42, s40
.Lsc_s2:
	s_add_u32 s40, s38, 0x3000
	buffer_load_dwordx4 v[108:111], v2, s[28:31], s40 offen nt
	s_waitcnt vmcnt(9)
	v_or3_b32 v12, v112, v113, v114
	v_bitop3_b32 v12, v12, s9, v115 bitop3:0xc8
	v_cmp_ne_u32_e32 vcc, 0, v12
	s_cbranch_vccz .Lsc_s3
	s_nop 0
	v_mbcnt_lo_u32_b32 v13, vcc_lo, 0
	v_mbcnt_hi_u32_b32 v13, vcc_hi, v13
	v_add_u32_e32 v13, s42, v13
	v_cmp_gt_i32_e64 s[0:1], s7, v13
	s_and_b64 s[4:5], vcc, s[0:1]
	s_and_saveexec_b64 s[0:1], s[4:5]
	v_lshl_add_u32 v14, v13, 4, v9
	v_lshl_add_u32 v15, v13, 2, v10
	v_add_u32_e32 v13, 0x300, v8
	ds_write_b128 v14, v[112:115]
	ds_write_b32 v15, v13
	s_mov_b64 exec, -1
	s_bcnt1_i32_b64 s40, vcc
	s_add_i32 s42, s42, s40
.Lsc_s3:
	s_add_u32 s40, s38, 0x3400
	buffer_load_dwordx4 v[112:115], v2, s[28:31], s40 offen nt
	s_waitcnt vmcnt(9)
	v_or3_b32 v12, v116, v117, v118
	v_bitop3_b32 v12, v12, s9, v119 bitop3:0xc8
	v_cmp_ne_u32_e32 vcc, 0, v12
	s_cbranch_vccz .Lsc_s4
	s_nop 0
	v_mbcnt_lo_u32_b32 v13, vcc_lo, 0
	v_mbcnt_hi_u32_b32 v13, vcc_hi, v13
	v_add_u32_e32 v13, s42, v13
	v_cmp_gt_i32_e64 s[0:1], s7, v13
	s_and_b64 s[4:5], vcc, s[0:1]
	s_and_saveexec_b64 s[0:1], s[4:5]
	v_lshl_add_u32 v14, v13, 4, v9
	v_lshl_add_u32 v15, v13, 2, v10
	v_add_u32_e32 v13, 0x400, v8
	ds_write_b128 v14, v[116:119]
	ds_write_b32 v15, v13
	s_mov_b64 exec, -1
	s_bcnt1_i32_b64 s40, vcc
	s_add_i32 s42, s42, s40
.Lsc_s4:
	s_add_u32 s40, s38, 0x3800
	buffer_load_dwordx4 v[116:119], v2, s[28:31], s40 offen nt
	s_waitcnt vmcnt(9)
	v_or3_b32 v12, v120, v121, v122
	v_bitop3_b32 v12, v12, s9, v123 bitop3:0xc8
	v_cmp_ne_u32_e32 vcc, 0, v12
	s_cbranch_vccz .Lsc_s5
	s_nop 0
	v_mbcnt_lo_u32_b32 v13, vcc_lo, 0
	v_mbcnt_hi_u32_b32 v13, vcc_hi, v13
	v_add_u32_e32 v13, s42, v13
	v_cmp_gt_i32_e64 s[0:1], s7, v13
	s_and_b64 s[4:5], vcc, s[0:1]
	s_and_saveexec_b64 s[0:1], s[4:5]
	v_lshl_add_u32 v14, v13, 4, v9
	v_lshl_add_u32 v15, v13, 2, v10
	v_add_u32_e32 v13, 0x500, v8
	ds_write_b128 v14, v[120:123]
	ds_write_b32 v15, v13
	s_mov_b64 exec, -1
	s_bcnt1_i32_b64 s40, vcc
	s_add_i32 s42, s42, s40
.Lsc_s5:
	s_add_u32 s40, s38, 0x3c00
	buffer_load_dwordx4 v[120:123], v2, s[28:31], s40 offen nt
	s_waitcnt vmcnt(9)
	v_or3_b32 v12, v124, v125, v126
	v_bitop3_b32 v12, v12, s9, v127 bitop3:0xc8
	v_cmp_ne_u32_e32 vcc, 0, v12
	s_cbranch_vccz .Lsc_s6
	s_nop 0
	v_mbcnt_lo_u32_b32 v13, vcc_lo, 0
	v_mbcnt_hi_u32_b32 v13, vcc_hi, v13
	v_add_u32_e32 v13, s42, v13
	v_cmp_gt_i32_e64 s[0:1], s7, v13
	s_and_b64 s[4:5], vcc, s[0:1]
	s_and_saveexec_b64 s[0:1], s[4:5]
	v_lshl_add_u32 v14, v13, 4, v9
	v_lshl_add_u32 v15, v13, 2, v10
	v_add_u32_e32 v13, 0x600, v8
	ds_write_b128 v14, v[124:127]
	ds_write_b32 v15, v13
	s_mov_b64 exec, -1
	s_bcnt1_i32_b64 s40, vcc
	s_add_i32 s42, s42, s40
.Lsc_s6:
	s_add_u32 s40, s38, 0x4000
	buffer_load_dwordx4 v[124:127], v2, s[28:31], s40 offen nt
	s_waitcnt vmcnt(9)
	v_or3_b32 v12, v128, v129, v130
	v_bitop3_b32 v12, v12, s9, v131 bitop3:0xc8
	v_cmp_ne_u32_e32 vcc, 0, v12
	s_cbranch_vccz .Lsc_s7
	s_nop 0
	v_mbcnt_lo_u32_b32 v13, vcc_lo, 0
	v_mbcnt_hi_u32_b32 v13, vcc_hi, v13
	v_add_u32_e32 v13, s42, v13
	v_cmp_gt_i32_e64 s[0:1], s7, v13
	s_and_b64 s[4:5], vcc, s[0:1]
	s_and_saveexec_b64 s[0:1], s[4:5]
	v_lshl_add_u32 v14, v13, 4, v9
	v_lshl_add_u32 v15, v13, 2, v10
	v_add_u32_e32 v13, 0x700, v8
	ds_write_b128 v14, v[128:131]
	ds_write_b32 v15, v13
	s_mov_b64 exec, -1
	s_bcnt1_i32_b64 s40, vcc
	s_add_i32 s42, s42, s40
.Lsc_s7:
	s_add_u32 s40, s38, 0x4400
	buffer_load_dwordx4 v[128:131], v2, s[28:31], s40 offen nt
	s_waitcnt vmcnt(9)
	v_or3_b32 v12, v132, v133, v134
	v_bitop3_b32 v12, v12, s9, v135 bitop3:0xc8
	v_cmp_ne_u32_e32 vcc, 0, v12
	s_cbranch_vccz .Lsc_s8
	s_nop 0
	v_mbcnt_lo_u32_b32 v13, vcc_lo, 0
	v_mbcnt_hi_u32_b32 v13, vcc_hi, v13
	v_add_u32_e32 v13, s42, v13
	v_cmp_gt_i32_e64 s[0:1], s7, v13
	s_and_b64 s[4:5], vcc, s[0:1]
	s_and_saveexec_b64 s[0:1], s[4:5]
	v_lshl_add_u32 v14, v13, 4, v9
	v_lshl_add_u32 v15, v13, 2, v10
	v_add_u32_e32 v13, 0x800, v8
	ds_write_b128 v14, v[132:135]
	ds_write_b32 v15, v13
	s_mov_b64 exec, -1
	s_bcnt1_i32_b64 s40, vcc
	s_add_i32 s42, s42, s40
.Lsc_s8:
	s_add_u32 s40, s38, 0x4800
	buffer_load_dwordx4 v[132:135], v2, s[28:31], s40 offen nt
	s_waitcnt vmcnt(9)
	v_or3_b32 v12, v136, v137, v138
	v_bitop3_b32 v12, v12, s9, v139 bitop3:0xc8
	v_cmp_ne_u32_e32 vcc, 0, v12
	s_cbranch_vccz .Lsc_s9
	s_nop 0
	v_mbcnt_lo_u32_b32 v13, vcc_lo, 0
	v_mbcnt_hi_u32_b32 v13, vcc_hi, v13
	v_add_u32_e32 v13, s42, v13
	v_cmp_gt_i32_e64 s[0:1], s7, v13
	s_and_b64 s[4:5], vcc, s[0:1]
	s_and_saveexec_b64 s[0:1], s[4:5]
	v_lshl_add_u32 v14, v13, 4, v9
	v_lshl_add_u32 v15, v13, 2, v10
	v_add_u32_e32 v13, 0x900, v8
	ds_write_b128 v14, v[136:139]
	ds_write_b32 v15, v13
	s_mov_b64 exec, -1
	s_bcnt1_i32_b64 s40, vcc
	s_add_i32 s42, s42, s40
.Lsc_s9:
	s_add_u32 s40, s38, 0x4c00
	buffer_load_dwordx4 v[136:139], v2, s[28:31], s40 offen nt
	s_waitcnt vmcnt(9)
	v_or3_b32 v12, v100, v101, v102
	v_bitop3_b32 v12, v12, s9, v103 bitop3:0xc8
	v_cmp_ne_u32_e32 vcc, 0, v12
	s_cbranch_vccz .Lsc_s10
	s_nop 0
	v_mbcnt_lo_u32_b32 v13, vcc_lo, 0
	v_mbcnt_hi_u32_b32 v13, vcc_hi, v13
	v_add_u32_e32 v13, s42, v13
	v_cmp_gt_i32_e64 s[0:1], s7, v13
	s_and_b64 s[4:5], vcc, s[0:1]
	s_and_saveexec_b64 s[0:1], s[4:5]
	v_lshl_add_u32 v14, v13, 4, v9
	v_lshl_add_u32 v15, v13, 2, v10
	v_add_u32_e32 v13, 0xa00, v8
	ds_write_b128 v14, v[100:103]
	ds_write_b32 v15, v13
	s_mov_b64 exec, -1
	s_bcnt1_i32_b64 s40, vcc
	s_add_i32 s42, s42, s40
.Lsc_s10:
	s_add_u32 s40, s38, 0x5000
	buffer_load_dwordx4 v[100:103], v2, s[28:31], s40 offen nt
	s_waitcnt vmcnt(9)
	v_or3_b32 v12, v104, v105, v106
	v_bitop3_b32 v12, v12, s9, v107 bitop3:0xc8
	v_cmp_ne_u32_e32 vcc, 0, v12
	s_cbranch_vccz .Lsc_s11
	s_nop 0
	v_mbcnt_lo_u32_b32 v13, vcc_lo, 0
	v_mbcnt_hi_u32_b32 v13, vcc_hi, v13
	v_add_u32_e32 v13, s42, v13
	v_cmp_gt_i32_e64 s[0:1], s7, v13
	s_and_b64 s[4:5], vcc, s[0:1]
	s_and_saveexec_b64 s[0:1], s[4:5]
	v_lshl_add_u32 v14, v13, 4, v9
	v_lshl_add_u32 v15, v13, 2, v10
	v_add_u32_e32 v13, 0xb00, v8
	ds_write_b128 v14, v[104:107]
	ds_write_b32 v15, v13
	s_mov_b64 exec, -1
	s_bcnt1_i32_b64 s40, vcc
	s_add_i32 s42, s42, s40
.Lsc_s11:
	s_add_u32 s40, s38, 0x5400
	buffer_load_dwordx4 v[104:107], v2, s[28:31], s40 offen nt
	s_waitcnt vmcnt(9)
	v_or3_b32 v12, v108, v109, v110
	v_bitop3_b32 v12, v12, s9, v111 bitop3:0xc8
	v_cmp_ne_u32_e32 vcc, 0, v12
	s_cbranch_vccz .Lsc_s12
	s_nop 0
	v_mbcnt_lo_u32_b32 v13, vcc_lo, 0
	v_mbcnt_hi_u32_b32 v13, vcc_hi, v13
	v_add_u32_e32 v13, s42, v13
	v_cmp_gt_i32_e64 s[0:1], s7, v13
	s_and_b64 s[4:5], vcc, s[0:1]
	s_and_saveexec_b64 s[0:1], s[4:5]
	v_lshl_add_u32 v14, v13, 4, v9
	v_lshl_add_u32 v15, v13, 2, v10
	v_add_u32_e32 v13, 0xc00, v8
	ds_write_b128 v14, v[108:111]
	ds_write_b32 v15, v13
	s_mov_b64 exec, -1
	s_bcnt1_i32_b64 s40, vcc
	s_add_i32 s42, s42, s40
.Lsc_s12:
	s_add_u32 s40, s38, 0x5800
	buffer_load_dwordx4 v[108:111], v2, s[28:31], s40 offen nt
	s_waitcnt vmcnt(9)
	v_or3_b32 v12, v112, v113, v114
	v_bitop3_b32 v12, v12, s9, v115 bitop3:0xc8
	v_cmp_ne_u32_e32 vcc, 0, v12
	s_cbranch_vccz .Lsc_s13
	s_nop 0
	v_mbcnt_lo_u32_b32 v13, vcc_lo, 0
	v_mbcnt_hi_u32_b32 v13, vcc_hi, v13
	v_add_u32_e32 v13, s42, v13
	v_cmp_gt_i32_e64 s[0:1], s7, v13
	s_and_b64 s[4:5], vcc, s[0:1]
	s_and_saveexec_b64 s[0:1], s[4:5]
	v_lshl_add_u32 v14, v13, 4, v9
	v_lshl_add_u32 v15, v13, 2, v10
	v_add_u32_e32 v13, 0xd00, v8
	ds_write_b128 v14, v[112:115]
	ds_write_b32 v15, v13
	s_mov_b64 exec, -1
	s_bcnt1_i32_b64 s40, vcc
	s_add_i32 s42, s42, s40
.Lsc_s13:
	s_add_u32 s40, s38, 0x5c00
	buffer_load_dwordx4 v[112:115], v2, s[28:31], s40 offen nt
	s_waitcnt vmcnt(9)
	v_or3_b32 v12, v116, v117, v118
	v_bitop3_b32 v12, v12, s9, v119 bitop3:0xc8
	v_cmp_ne_u32_e32 vcc, 0, v12
	s_cbranch_vccz .Lsc_s14
	s_nop 0
	v_mbcnt_lo_u32_b32 v13, vcc_lo, 0
	v_mbcnt_hi_u32_b32 v13, vcc_hi, v13
	v_add_u32_e32 v13, s42, v13
	v_cmp_gt_i32_e64 s[0:1], s7, v13
	s_and_b64 s[4:5], vcc, s[0:1]
	s_and_saveexec_b64 s[0:1], s[4:5]
	v_lshl_add_u32 v14, v13, 4, v9
	v_lshl_add_u32 v15, v13, 2, v10
	v_add_u32_e32 v13, 0xe00, v8
	ds_write_b128 v14, v[116:119]
	ds_write_b32 v15, v13
	s_mov_b64 exec, -1
	s_bcnt1_i32_b64 s40, vcc
	s_add_i32 s42, s42, s40
.Lsc_s14:
	s_add_u32 s40, s38, 0x6000
	buffer_load_dwordx4 v[116:119], v2, s[28:31], s40 offen nt
	s_waitcnt vmcnt(9)
	v_or3_b32 v12, v120, v121, v122
	v_bitop3_b32 v12, v12, s9, v123 bitop3:0xc8
	v_cmp_ne_u32_e32 vcc, 0, v12
	s_cbranch_vccz .Lsc_s15
	s_nop 0
	v_mbcnt_lo_u32_b32 v13, vcc_lo, 0
	v_mbcnt_hi_u32_b32 v13, vcc_hi, v13
	v_add_u32_e32 v13, s42, v13
	v_cmp_gt_i32_e64 s[0:1], s7, v13
	s_and_b64 s[4:5], vcc, s[0:1]
	s_and_saveexec_b64 s[0:1], s[4:5]
	v_lshl_add_u32 v14, v13, 4, v9
	v_lshl_add_u32 v15, v13, 2, v10
	v_add_u32_e32 v13, 0xf00, v8
	ds_write_b128 v14, v[120:123]
	ds_write_b32 v15, v13
	s_mov_b64 exec, -1
	s_bcnt1_i32_b64 s40, vcc
	s_add_i32 s42, s42, s40
.Lsc_s15:
	s_add_u32 s40, s38, 0x6400
	buffer_load_dwordx4 v[120:123], v2, s[28:31], s40 offen nt
	s_waitcnt vmcnt(9)
	v_or3_b32 v12, v124, v125, v126
	v_bitop3_b32 v12, v12, s9, v127 bitop3:0xc8
	v_cmp_ne_u32_e32 vcc, 0, v12
	s_cbranch_vccz .Lsc_s16
	s_nop 0
	v_mbcnt_lo_u32_b32 v13, vcc_lo, 0
	v_mbcnt_hi_u32_b32 v13, vcc_hi, v13
	v_add_u32_e32 v13, s42, v13
	v_cmp_gt_i32_e64 s[0:1], s7, v13
	s_and_b64 s[4:5], vcc, s[0:1]
	s_and_saveexec_b64 s[0:1], s[4:5]
	v_lshl_add_u32 v14, v13, 4, v9
	v_lshl_add_u32 v15, v13, 2, v10
	v_add_u32_e32 v13, 0x1000, v8
	ds_write_b128 v14, v[124:127]
	ds_write_b32 v15, v13
	s_mov_b64 exec, -1
	s_bcnt1_i32_b64 s40, vcc
	s_add_i32 s42, s42, s40
.Lsc_s16:
	s_add_u32 s40, s38, 0x6800
	buffer_load_dwordx4 v[124:127], v2, s[28:31], s40 offen nt
	s_waitcnt vmcnt(9)
	v_or3_b32 v12, v128, v129, v130
	v_bitop3_b32 v12, v12, s9, v131 bitop3:0xc8
	v_cmp_ne_u32_e32 vcc, 0, v12
	s_cbranch_vccz .Lsc_s17
	s_nop 0
	v_mbcnt_lo_u32_b32 v13, vcc_lo, 0
	v_mbcnt_hi_u32_b32 v13, vcc_hi, v13
	v_add_u32_e32 v13, s42, v13
	v_cmp_gt_i32_e64 s[0:1], s7, v13
	s_and_b64 s[4:5], vcc, s[0:1]
	s_and_saveexec_b64 s[0:1], s[4:5]
	v_lshl_add_u32 v14, v13, 4, v9
	v_lshl_add_u32 v15, v13, 2, v10
	v_add_u32_e32 v13, 0x1100, v8
	ds_write_b128 v14, v[128:131]
	ds_write_b32 v15, v13
	s_mov_b64 exec, -1
	s_bcnt1_i32_b64 s40, vcc
	s_add_i32 s42, s42, s40
.Lsc_s17:
	s_add_u32 s40, s38, 0x6c00
	buffer_load_dwordx4 v[128:131], v2, s[28:31], s40 offen nt
	s_waitcnt vmcnt(9)
	v_or3_b32 v12, v132, v133, v134
	v_bitop3_b32 v12, v12, s9, v135 bitop3:0xc8
	v_cmp_ne_u32_e32 vcc, 0, v12
	s_cbranch_vccz .Lsc_s18
	s_nop 0
	v_mbcnt_lo_u32_b32 v13, vcc_lo, 0
	v_mbcnt_hi_u32_b32 v13, vcc_hi, v13
	v_add_u32_e32 v13, s42, v13
	v_cmp_gt_i32_e64 s[0:1], s7, v13
	s_and_b64 s[4:5], vcc, s[0:1]
	s_and_saveexec_b64 s[0:1], s[4:5]
	v_lshl_add_u32 v14, v13, 4, v9
	v_lshl_add_u32 v15, v13, 2, v10
	v_add_u32_e32 v13, 0x1200, v8
	ds_write_b128 v14, v[132:135]
	ds_write_b32 v15, v13
	s_mov_b64 exec, -1
	s_bcnt1_i32_b64 s40, vcc
	s_add_i32 s42, s42, s40
.Lsc_s18:
	s_add_u32 s40, s38, 0x7000
	buffer_load_dwordx4 v[132:135], v2, s[28:31], s40 offen nt
	s_waitcnt vmcnt(9)
	v_or3_b32 v12, v136, v137, v138
	v_bitop3_b32 v12, v12, s9, v139 bitop3:0xc8
	v_cmp_ne_u32_e32 vcc, 0, v12
	s_cbranch_vccz .Lsc_s19
	s_nop 0
	v_mbcnt_lo_u32_b32 v13, vcc_lo, 0
	v_mbcnt_hi_u32_b32 v13, vcc_hi, v13
	v_add_u32_e32 v13, s42, v13
	v_cmp_gt_i32_e64 s[0:1], s7, v13
	s_and_b64 s[4:5], vcc, s[0:1]
	s_and_saveexec_b64 s[0:1], s[4:5]
	v_lshl_add_u32 v14, v13, 4, v9
	v_lshl_add_u32 v15, v13, 2, v10
	v_add_u32_e32 v13, 0x1300, v8
	ds_write_b128 v14, v[136:139]
	ds_write_b32 v15, v13
	s_mov_b64 exec, -1
	s_bcnt1_i32_b64 s40, vcc
	s_add_i32 s42, s42, s40
.Lsc_s19:
	s_add_u32 s40, s38, 0x7400
	buffer_load_dwordx4 v[136:139], v2, s[28:31], s40 offen nt
	s_waitcnt vmcnt(9)
	v_or3_b32 v12, v100, v101, v102
	v_bitop3_b32 v12, v12, s9, v103 bitop3:0xc8
	v_cmp_ne_u32_e32 vcc, 0, v12
	s_cbranch_vccz .Lsc_s20
	s_nop 0
	v_mbcnt_lo_u32_b32 v13, vcc_lo, 0
	v_mbcnt_hi_u32_b32 v13, vcc_hi, v13
	v_add_u32_e32 v13, s42, v13
	v_cmp_gt_i32_e64 s[0:1], s7, v13
	s_and_b64 s[4:5], vcc, s[0:1]
	s_and_saveexec_b64 s[0:1], s[4:5]
	v_lshl_add_u32 v14, v13, 4, v9
	v_lshl_add_u32 v15, v13, 2, v10
	v_add_u32_e32 v13, 0x1400, v8
	ds_write_b128 v14, v[100:103]
	ds_write_b32 v15, v13
	s_mov_b64 exec, -1
	s_bcnt1_i32_b64 s40, vcc
	s_add_i32 s42, s42, s40
.Lsc_s20:
	s_add_u32 s40, s38, 0x7800
	buffer_load_dwordx4 v[100:103], v2, s[28:31], s40 offen nt
	s_waitcnt vmcnt(9)
	v_or3_b32 v12, v104, v105, v106
	v_bitop3_b32 v12, v12, s9, v107 bitop3:0xc8
	v_cmp_ne_u32_e32 vcc, 0, v12
	s_cbranch_vccz .Lsc_s21
	s_nop 0
	v_mbcnt_lo_u32_b32 v13, vcc_lo, 0
	v_mbcnt_hi_u32_b32 v13, vcc_hi, v13
	v_add_u32_e32 v13, s42, v13
	v_cmp_gt_i32_e64 s[0:1], s7, v13
	s_and_b64 s[4:5], vcc, s[0:1]
	s_and_saveexec_b64 s[0:1], s[4:5]
	v_lshl_add_u32 v14, v13, 4, v9
	v_lshl_add_u32 v15, v13, 2, v10
	v_add_u32_e32 v13, 0x1500, v8
	ds_write_b128 v14, v[104:107]
	ds_write_b32 v15, v13
	s_mov_b64 exec, -1
	s_bcnt1_i32_b64 s40, vcc
	s_add_i32 s42, s42, s40
.Lsc_s21:
	s_add_u32 s40, s38, 0x7c00
	buffer_load_dwordx4 v[104:107], v2, s[28:31], s40 offen nt
	s_waitcnt vmcnt(9)
	v_or3_b32 v12, v108, v109, v110
	v_bitop3_b32 v12, v12, s9, v111 bitop3:0xc8
	v_cmp_ne_u32_e32 vcc, 0, v12
	s_cbranch_vccz .Lsc_s22
	s_nop 0
	v_mbcnt_lo_u32_b32 v13, vcc_lo, 0
	v_mbcnt_hi_u32_b32 v13, vcc_hi, v13
	v_add_u32_e32 v13, s42, v13
	v_cmp_gt_i32_e64 s[0:1], s7, v13
	s_and_b64 s[4:5], vcc, s[0:1]
	s_and_saveexec_b64 s[0:1], s[4:5]
	v_lshl_add_u32 v14, v13, 4, v9
	v_lshl_add_u32 v15, v13, 2, v10
	v_add_u32_e32 v13, 0x1600, v8
	ds_write_b128 v14, v[108:111]
	ds_write_b32 v15, v13
	s_mov_b64 exec, -1
	s_bcnt1_i32_b64 s40, vcc
	s_add_i32 s42, s42, s40
.Lsc_s22:
	s_add_u32 s40, s38, 0x8000
	buffer_load_dwordx4 v[108:111], v2, s[28:31], s40 offen nt
	s_waitcnt vmcnt(9)
	v_or3_b32 v12, v112, v113, v114
	v_bitop3_b32 v12, v12, s9, v115 bitop3:0xc8
	v_cmp_ne_u32_e32 vcc, 0, v12
	s_cbranch_vccz .Lsc_s23
	s_nop 0
	v_mbcnt_lo_u32_b32 v13, vcc_lo, 0
	v_mbcnt_hi_u32_b32 v13, vcc_hi, v13
	v_add_u32_e32 v13, s42, v13
	v_cmp_gt_i32_e64 s[0:1], s7, v13
	s_and_b64 s[4:5], vcc, s[0:1]
	s_and_saveexec_b64 s[0:1], s[4:5]
	v_lshl_add_u32 v14, v13, 4, v9
	v_lshl_add_u32 v15, v13, 2, v10
	v_add_u32_e32 v13, 0x1700, v8
	ds_write_b128 v14, v[112:115]
	ds_write_b32 v15, v13
	s_mov_b64 exec, -1
	s_bcnt1_i32_b64 s40, vcc
	s_add_i32 s42, s42, s40
.Lsc_s23:
	s_add_u32 s40, s38, 0x8400
	buffer_load_dwordx4 v[112:115], v2, s[28:31], s40 offen nt
	s_waitcnt vmcnt(9)
	v_or3_b32 v12, v116, v117, v118
	v_bitop3_b32 v12, v12, s9, v119 bitop3:0xc8
	v_cmp_ne_u32_e32 vcc, 0, v12
	s_cbranch_vccz .Lsc_s24
	s_nop 0
	v_mbcnt_lo_u32_b32 v13, vcc_lo, 0
	v_mbcnt_hi_u32_b32 v13, vcc_hi, v13
	v_add_u32_e32 v13, s42, v13
	v_cmp_gt_i32_e64 s[0:1], s7, v13
	s_and_b64 s[4:5], vcc, s[0:1]
	s_and_saveexec_b64 s[0:1], s[4:5]
	v_lshl_add_u32 v14, v13, 4, v9
	v_lshl_add_u32 v15, v13, 2, v10
	v_add_u32_e32 v13, 0x1800, v8
	ds_write_b128 v14, v[116:119]
	ds_write_b32 v15, v13
	s_mov_b64 exec, -1
	s_bcnt1_i32_b64 s40, vcc
	s_add_i32 s42, s42, s40
.Lsc_s24:
	s_add_u32 s40, s38, 0x8800
	buffer_load_dwordx4 v[116:119], v2, s[28:31], s40 offen nt
	s_waitcnt vmcnt(9)
	v_or3_b32 v12, v120, v121, v122
	v_bitop3_b32 v12, v12, s9, v123 bitop3:0xc8
	v_cmp_ne_u32_e32 vcc, 0, v12
	s_cbranch_vccz .Lsc_s25
	s_nop 0
	v_mbcnt_lo_u32_b32 v13, vcc_lo, 0
	v_mbcnt_hi_u32_b32 v13, vcc_hi, v13
	v_add_u32_e32 v13, s42, v13
	v_cmp_gt_i32_e64 s[0:1], s7, v13
	s_and_b64 s[4:5], vcc, s[0:1]
	s_and_saveexec_b64 s[0:1], s[4:5]
	v_lshl_add_u32 v14, v13, 4, v9
	v_lshl_add_u32 v15, v13, 2, v10
	v_add_u32_e32 v13, 0x1900, v8
	ds_write_b128 v14, v[120:123]
	ds_write_b32 v15, v13
	s_mov_b64 exec, -1
	s_bcnt1_i32_b64 s40, vcc
	s_add_i32 s42, s42, s40
.Lsc_s25:
	s_add_u32 s40, s38, 0x8c00
	buffer_load_dwordx4 v[120:123], v2, s[28:31], s40 offen nt
	s_waitcnt vmcnt(9)
	v_or3_b32 v12, v124, v125, v126
	v_bitop3_b32 v12, v12, s9, v127 bitop3:0xc8
	v_cmp_ne_u32_e32 vcc, 0, v12
	s_cbranch_vccz .Lsc_s26
	s_nop 0
	v_mbcnt_lo_u32_b32 v13, vcc_lo, 0
	v_mbcnt_hi_u32_b32 v13, vcc_hi, v13
	v_add_u32_e32 v13, s42, v13
	v_cmp_gt_i32_e64 s[0:1], s7, v13
	s_and_b64 s[4:5], vcc, s[0:1]
	s_and_saveexec_b64 s[0:1], s[4:5]
	v_lshl_add_u32 v14, v13, 4, v9
	v_lshl_add_u32 v15, v13, 2, v10
	v_add_u32_e32 v13, 0x1a00, v8
	ds_write_b128 v14, v[124:127]
	ds_write_b32 v15, v13
	s_mov_b64 exec, -1
	s_bcnt1_i32_b64 s40, vcc
	s_add_i32 s42, s42, s40
.Lsc_s26:
	s_add_u32 s40, s38, 0x9000
	buffer_load_dwordx4 v[124:127], v2, s[28:31], s40 offen nt
	s_waitcnt vmcnt(9)
	v_or3_b32 v12, v128, v129, v130
	v_bitop3_b32 v12, v12, s9, v131 bitop3:0xc8
	v_cmp_ne_u32_e32 vcc, 0, v12
	s_cbranch_vccz .Lsc_s27
	s_nop 0
	v_mbcnt_lo_u32_b32 v13, vcc_lo, 0
	v_mbcnt_hi_u32_b32 v13, vcc_hi, v13
	v_add_u32_e32 v13, s42, v13
	v_cmp_gt_i32_e64 s[0:1], s7, v13
	s_and_b64 s[4:5], vcc, s[0:1]
	s_and_saveexec_b64 s[0:1], s[4:5]
	v_lshl_add_u32 v14, v13, 4, v9
	v_lshl_add_u32 v15, v13, 2, v10
	v_add_u32_e32 v13, 0x1b00, v8
	ds_write_b128 v14, v[128:131]
	ds_write_b32 v15, v13
	s_mov_b64 exec, -1
	s_bcnt1_i32_b64 s40, vcc
	s_add_i32 s42, s42, s40
.Lsc_s27:
	s_add_u32 s40, s38, 0x9400
	buffer_load_dwordx4 v[128:131], v2, s[28:31], s40 offen nt
	s_waitcnt vmcnt(9)
	v_or3_b32 v12, v132, v133, v134
	v_bitop3_b32 v12, v12, s9, v135 bitop3:0xc8
	v_cmp_ne_u32_e32 vcc, 0, v12
	s_cbranch_vccz .Lsc_s28
	s_nop 0
	v_mbcnt_lo_u32_b32 v13, vcc_lo, 0
	v_mbcnt_hi_u32_b32 v13, vcc_hi, v13
	v_add_u32_e32 v13, s42, v13
	v_cmp_gt_i32_e64 s[0:1], s7, v13
	s_and_b64 s[4:5], vcc, s[0:1]
	s_and_saveexec_b64 s[0:1], s[4:5]
	v_lshl_add_u32 v14, v13, 4, v9
	v_lshl_add_u32 v15, v13, 2, v10
	v_add_u32_e32 v13, 0x1c00, v8
	ds_write_b128 v14, v[132:135]
	ds_write_b32 v15, v13
	s_mov_b64 exec, -1
	s_bcnt1_i32_b64 s40, vcc
	s_add_i32 s42, s42, s40
.Lsc_s28:
	s_add_u32 s40, s38, 0x9800
	buffer_load_dwordx4 v[132:135], v2, s[28:31], s40 offen nt
	s_waitcnt vmcnt(9)
	v_or3_b32 v12, v136, v137, v138
	v_bitop3_b32 v12, v12, s9, v139 bitop3:0xc8
	v_cmp_ne_u32_e32 vcc, 0, v12
	s_cbranch_vccz .Lsc_s29
	s_nop 0
	v_mbcnt_lo_u32_b32 v13, vcc_lo, 0
	v_mbcnt_hi_u32_b32 v13, vcc_hi, v13
	v_add_u32_e32 v13, s42, v13
	v_cmp_gt_i32_e64 s[0:1], s7, v13
	s_and_b64 s[4:5], vcc, s[0:1]
	s_and_saveexec_b64 s[0:1], s[4:5]
	v_lshl_add_u32 v14, v13, 4, v9
	v_lshl_add_u32 v15, v13, 2, v10
	v_add_u32_e32 v13, 0x1d00, v8
	ds_write_b128 v14, v[136:139]
	ds_write_b32 v15, v13
	s_mov_b64 exec, -1
	s_bcnt1_i32_b64 s40, vcc
	s_add_i32 s42, s42, s40
.Lsc_s29:
	s_add_u32 s40, s38, 0x9c00
	buffer_load_dwordx4 v[136:139], v4, s[28:31], s40 offen nt
	s_waitcnt vmcnt(9)
	v_or3_b32 v12, v100, v101, v102
	v_bitop3_b32 v12, v12, s9, v103 bitop3:0xc8
	v_cmp_ne_u32_e32 vcc, 0, v12
	s_cbranch_vccz .Lsc_s30
	s_nop 0
	v_mbcnt_lo_u32_b32 v13, vcc_lo, 0
	v_mbcnt_hi_u32_b32 v13, vcc_hi, v13
	v_add_u32_e32 v13, s42, v13
	v_cmp_gt_i32_e64 s[0:1], s7, v13
	s_and_b64 s[4:5], vcc, s[0:1]
	s_and_saveexec_b64 s[0:1], s[4:5]
	v_lshl_add_u32 v14, v13, 4, v9
	v_lshl_add_u32 v15, v13, 2, v10
	v_add_u32_e32 v13, 0x1e00, v8
	ds_write_b128 v14, v[100:103]
	ds_write_b32 v15, v13
	s_mov_b64 exec, -1
	s_bcnt1_i32_b64 s40, vcc
	s_add_i32 s42, s42, s40
.Lsc_s30:
	s_mov_b32 s40, s39
	buffer_load_dwordx4 v[100:103], v5, s[28:31], s40 offen nt
	s_waitcnt vmcnt(9)
	v_or3_b32 v12, v104, v105, v106
	v_bitop3_b32 v12, v12, s9, v107 bitop3:0xc8
	v_cmp_ne_u32_e32 vcc, 0, v12
	s_cbranch_vccz .Lsc_s31
	s_nop 0
	v_mbcnt_lo_u32_b32 v13, vcc_lo, 0
	v_mbcnt_hi_u32_b32 v13, vcc_hi, v13
	v_add_u32_e32 v13, s42, v13
	v_cmp_gt_i32_e64 s[0:1], s7, v13
	s_and_b64 s[4:5], vcc, s[0:1]
	s_and_saveexec_b64 s[0:1], s[4:5]
	v_lshl_add_u32 v14, v13, 4, v9
	v_lshl_add_u32 v15, v13, 2, v10
	v_add_u32_e32 v13, 0x1f00, v8
	ds_write_b128 v14, v[104:107]
	ds_write_b32 v15, v13
	s_mov_b64 exec, -1
	s_bcnt1_i32_b64 s40, vcc
	s_add_i32 s42, s42, s40
.Lsc_s31:
	s_add_u32 s40, s39, 0x400
	buffer_load_dwordx4 v[104:107], v6, s[28:31], s40 offen nt
	s_waitcnt vmcnt(9)
	v_or3_b32 v12, v108, v109, v110
	v_bitop3_b32 v12, v12, s9, v111 bitop3:0xc8
	v_cmp_ne_u32_e32 vcc, 0, v12
	s_cbranch_vccz .Lsc_s32
	s_nop 0
	v_mbcnt_lo_u32_b32 v13, vcc_lo, 0
	v_mbcnt_hi_u32_b32 v13, vcc_hi, v13
	v_add_u32_e32 v13, s42, v13
	v_cmp_gt_i32_e64 s[0:1], s7, v13
	s_and_b64 s[4:5], vcc, s[0:1]
	s_and_saveexec_b64 s[0:1], s[4:5]
	v_lshl_add_u32 v14, v13, 4, v9
	v_lshl_add_u32 v15, v13, 2, v10
	v_add_u32_e32 v13, 0x2000, v8
	ds_write_b128 v14, v[108:111]
	ds_write_b32 v15, v13
	s_mov_b64 exec, -1
	s_bcnt1_i32_b64 s40, vcc
	s_add_i32 s42, s42, s40
.Lsc_s32:
	s_add_u32 s40, s39, 0x800
	buffer_load_dwordx4 v[108:111], v6, s[28:31], s40 offen nt
	s_waitcnt vmcnt(9)
	v_or3_b32 v12, v112, v113, v114
	v_bitop3_b32 v12, v12, s9, v115 bitop3:0xc8
	v_cmp_ne_u32_e32 vcc, 0, v12
	s_cbranch_vccz .Lsc_s33
	s_nop 0
	v_mbcnt_lo_u32_b32 v13, vcc_lo, 0
	v_mbcnt_hi_u32_b32 v13, vcc_hi, v13
	v_add_u32_e32 v13, s42, v13
	v_cmp_gt_i32_e64 s[0:1], s7, v13
	s_and_b64 s[4:5], vcc, s[0:1]
	s_and_saveexec_b64 s[0:1], s[4:5]
	v_lshl_add_u32 v14, v13, 4, v9
	v_lshl_add_u32 v15, v13, 2, v10
	v_add_u32_e32 v13, 0x2100, v8
	ds_write_b128 v14, v[112:115]
	ds_write_b32 v15, v13
	s_mov_b64 exec, -1
	s_bcnt1_i32_b64 s40, vcc
	s_add_i32 s42, s42, s40
.Lsc_s33:
	s_add_u32 s40, s39, 0xc00
	buffer_load_dwordx4 v[112:115], v6, s[28:31], s40 offen nt
	s_waitcnt vmcnt(9)
	v_or3_b32 v12, v116, v117, v118
	v_bitop3_b32 v12, v12, s9, v119 bitop3:0xc8
	v_cmp_ne_u32_e32 vcc, 0, v12
	s_cbranch_vccz .Lsc_s34
	s_nop 0
	v_mbcnt_lo_u32_b32 v13, vcc_lo, 0
	v_mbcnt_hi_u32_b32 v13, vcc_hi, v13
	v_add_u32_e32 v13, s42, v13
	v_cmp_gt_i32_e64 s[0:1], s7, v13
	s_and_b64 s[4:5], vcc, s[0:1]
	s_and_saveexec_b64 s[0:1], s[4:5]
	v_lshl_add_u32 v14, v13, 4, v9
	v_lshl_add_u32 v15, v13, 2, v10
	v_add_u32_e32 v13, 0x2200, v8
	ds_write_b128 v14, v[116:119]
	ds_write_b32 v15, v13
	s_mov_b64 exec, -1
	s_bcnt1_i32_b64 s40, vcc
	s_add_i32 s42, s42, s40
.Lsc_s34:
	s_add_u32 s40, s39, 0x1000
	buffer_load_dwordx4 v[116:119], v6, s[28:31], s40 offen nt
	s_waitcnt vmcnt(9)
	v_or3_b32 v12, v120, v121, v122
	v_bitop3_b32 v12, v12, s9, v123 bitop3:0xc8
	v_cmp_ne_u32_e32 vcc, 0, v12
	s_cbranch_vccz .Lsc_s35
	s_nop 0
	v_mbcnt_lo_u32_b32 v13, vcc_lo, 0
	v_mbcnt_hi_u32_b32 v13, vcc_hi, v13
	v_add_u32_e32 v13, s42, v13
	v_cmp_gt_i32_e64 s[0:1], s7, v13
	s_and_b64 s[4:5], vcc, s[0:1]
	s_and_saveexec_b64 s[0:1], s[4:5]
	v_lshl_add_u32 v14, v13, 4, v9
	v_lshl_add_u32 v15, v13, 2, v10
	v_add_u32_e32 v13, 0x2300, v8
	ds_write_b128 v14, v[120:123]
	ds_write_b32 v15, v13
	s_mov_b64 exec, -1
	s_bcnt1_i32_b64 s40, vcc
	s_add_i32 s42, s42, s40
.Lsc_s35:
	s_add_u32 s40, s39, 0x1400
	buffer_load_dwordx4 v[120:123], v6, s[28:31], s40 offen nt
	s_waitcnt vmcnt(9)
	v_or3_b32 v12, v124, v125, v126
	v_bitop3_b32 v12, v12, s9, v127 bitop3:0xc8
	v_cmp_ne_u32_e32 vcc, 0, v12
	s_cbranch_vccz .Lsc_s36
	s_nop 0
	v_mbcnt_lo_u32_b32 v13, vcc_lo, 0
	v_mbcnt_hi_u32_b32 v13, vcc_hi, v13
	v_add_u32_e32 v13, s42, v13
	v_cmp_gt_i32_e64 s[0:1], s7, v13
	s_and_b64 s[4:5], vcc, s[0:1]
	s_and_saveexec_b64 s[0:1], s[4:5]
	v_lshl_add_u32 v14, v13, 4, v9
	v_lshl_add_u32 v15, v13, 2, v10
	v_add_u32_e32 v13, 0x2400, v8
	ds_write_b128 v14, v[124:127]
	ds_write_b32 v15, v13
	s_mov_b64 exec, -1
	s_bcnt1_i32_b64 s40, vcc
	s_add_i32 s42, s42, s40
.Lsc_s36:
	s_add_u32 s40, s39, 0x1800
	buffer_load_dwordx4 v[124:127], v6, s[28:31], s40 offen nt
	s_waitcnt vmcnt(9)
	v_or3_b32 v12, v128, v129, v130
	v_bitop3_b32 v12, v12, s9, v131 bitop3:0xc8
	v_cmp_ne_u32_e32 vcc, 0, v12
	s_cbranch_vccz .Lsc_s37
	s_nop 0
	v_mbcnt_lo_u32_b32 v13, vcc_lo, 0
	v_mbcnt_hi_u32_b32 v13, vcc_hi, v13
	v_add_u32_e32 v13, s42, v13
	v_cmp_gt_i32_e64 s[0:1], s7, v13
	s_and_b64 s[4:5], vcc, s[0:1]
	s_and_saveexec_b64 s[0:1], s[4:5]
	v_lshl_add_u32 v14, v13, 4, v9
	v_lshl_add_u32 v15, v13, 2, v10
	v_add_u32_e32 v13, 0x2500, v8
	ds_write_b128 v14, v[128:131]
	ds_write_b32 v15, v13
	s_mov_b64 exec, -1
	s_bcnt1_i32_b64 s40, vcc
	s_add_i32 s42, s42, s40
.Lsc_s37:
	s_add_u32 s40, s39, 0x1c00
	buffer_load_dwordx4 v[128:131], v6, s[28:31], s40 offen nt
	s_waitcnt vmcnt(9)
	v_or3_b32 v12, v132, v133, v134
	v_bitop3_b32 v12, v12, s9, v135 bitop3:0xc8
	v_cmp_ne_u32_e32 vcc, 0, v12
	s_cbranch_vccz .Lsc_s38
	s_nop 0
	v_mbcnt_lo_u32_b32 v13, vcc_lo, 0
	v_mbcnt_hi_u32_b32 v13, vcc_hi, v13
	v_add_u32_e32 v13, s42, v13
	v_cmp_gt_i32_e64 s[0:1], s7, v13
	s_and_b64 s[4:5], vcc, s[0:1]
	s_and_saveexec_b64 s[0:1], s[4:5]
	v_lshl_add_u32 v14, v13, 4, v9
	v_lshl_add_u32 v15, v13, 2, v10
	v_add_u32_e32 v13, 0x2600, v8
	ds_write_b128 v14, v[132:135]
	ds_write_b32 v15, v13
	s_mov_b64 exec, -1
	s_bcnt1_i32_b64 s40, vcc
	s_add_i32 s42, s42, s40
.Lsc_s38:
	s_add_u32 s40, s39, 0x2000
	buffer_load_dwordx4 v[132:135], v6, s[28:31], s40 offen nt
	s_waitcnt vmcnt(9)
	v_or3_b32 v12, v136, v137, v138
	v_bitop3_b32 v12, v12, s9, v139 bitop3:0xc8
	v_cmp_ne_u32_e32 vcc, 0, v12
	s_and_b64 vcc, vcc, s[50:51]
	s_cbranch_vccz .Lsc_s39
	s_nop 0
	v_mbcnt_lo_u32_b32 v13, vcc_lo, 0
	v_mbcnt_hi_u32_b32 v13, vcc_hi, v13
	v_add_u32_e32 v13, s42, v13
	v_cmp_gt_i32_e64 s[0:1], s7, v13
	s_and_b64 s[4:5], vcc, s[0:1]
	s_and_saveexec_b64 s[0:1], s[4:5]
	v_lshl_add_u32 v14, v13, 4, v9
	v_lshl_add_u32 v15, v13, 2, v10
	v_add_u32_e32 v13, 0x2700, v8
	ds_write_b128 v14, v[136:139]
	ds_write_b32 v15, v13
	s_mov_b64 exec, -1
	s_bcnt1_i32_b64 s40, vcc
	s_add_i32 s42, s42, s40
.Lsc_s39:
	s_add_u32 s40, s39, 0x2400
	buffer_load_dwordx4 v[136:139], v6, s[28:31], s40 offen nt
	s_waitcnt lgkmcnt(0)
	s_add_i32 s42, s42, 1
	v_mov_b32_e32 v12, s42
	ds_write_b32 v11, v12
	s_cmp_eq_u32 s35, s36
	s_cbranch_scc1 .LBB1_384
	s_add_i32 s35, s35, 1
	s_mov_b32 s37, s52
	s_mov_b32 s38, s39
	s_mov_b32 s47, s53
	s_branch .Lsc_row
